# MoeOrder::next: tstart[e], tstart[e+1] via v_readlane from the searched vector (no second LDS read), group division by shift / multiply for group size <= 4 (11 sites); moe_combine loop-top store-drain
# speedup vs baseline: 1.0078x; 1.0078x over previous
.LBB0_33:
	s_waitcnt vmcnt(0)
	v_lshlrev_b32_e32 v182, 4, v192
	v_and_b32_e32 v183, 15, v194
	s_and_b64 vcc, exec, s[36:37]
	s_cbranch_vccz .LBB0_56
	s_ashr_i32 s5, s4, 31
	v_mov_b32_e32 v2, s4
	v_mov_b32_e32 v3, s5
	v_cmp_ge_i64_e32 vcc, s[26:27], v[2:3]
	s_cbranch_vccnz .LBB0_56
	v_ashrrev_i32_e32 v0, 31, v192
	v_lshrrev_b32_e32 v0, 26, v0
	v_add_u32_e32 v0, v192, v0
	v_ashrrev_i32_e32 v10, 6, v0
	v_ashrrev_i32_e32 v0, 31, v182
	v_lshrrev_b32_e32 v0, 22, v0
	v_add_u32_e32 v0, v182, v0
	v_and_b32_e32 v0, 0xfffffc00, v0
	v_sub_u32_e32 v0, v182, v0
	v_lshrrev_b32_e32 v2, 4, v0
	v_bitop3_b32 v2, v2, v0, 32 bitop3:0x6c
	v_ashrrev_i32_e32 v0, 31, v0
	v_lshrrev_b32_e32 v0, 26, v0
	v_add_u32_e32 v0, v2, v0
	s_add_u32 s14, s30, 0x39000000
	v_lshlrev_b32_e32 v3, 3, v10
	v_ashrrev_i32_e32 v11, 6, v0
	v_and_b32_e32 v0, 0xc0, v0
	s_addc_u32 s15, s31, 0
	s_ashr_i32 s83, s82, 31
	v_and_b32_e32 v3, -16, v3
	v_sub_u32_e32 v0, v2, v0
	s_lshl_b64 s[4:5], s[82:83], 25
	v_add_u32_e32 v3, v11, v3
	v_ashrrev_i16_sdwa v0, v225, sext(v0) dst_sel:DWORD dst_unused:UNUSED_PAD src0_sel:DWORD src1_sel:BYTE_0
	s_add_u32 s16, s70, s4
	v_lshlrev_b32_e32 v4, 5, v10
	v_bfe_i32 v12, v0, 0, 16
	v_lshlrev_b32_e32 v0, 1, v3
	v_lshrrev_b32_e32 v2, 2, v3
	v_and_b32_e32 v5, 3, v11
	s_mov_b32 s4, 0x3fffe0
	v_and_b32_e32 v4, 32, v4
	v_and_b32_e32 v0, 24, v0
	v_and_b32_e32 v2, 4, v2
	v_and_or_b32 v5, v3, s4, v5
	v_or3_b32 v0, v5, v2, v0
	v_add_lshl_u32 v2, v4, v12, 1
	v_lshl_add_u32 v162, v3, 10, v2
	v_lshl_add_u32 v0, v0, 10, v2
	v_add_u32_e32 v2, 0x2000, v182
	v_ashrrev_i32_e32 v3, 31, v2
	v_lshrrev_b32_e32 v3, 22, v3
	v_add_u32_e32 v3, v2, v3
	v_ashrrev_i32_e32 v13, 10, v3
	v_mul_i32_i24_e32 v3, 0x400, v13
	v_sub_u32_e32 v2, v2, v3
	v_lshrrev_b32_e32 v3, 4, v2
	v_bitop3_b32 v2, v3, v2, 32 bitop3:0x6c
	v_ashrrev_i32_e32 v4, 31, v2
	v_lshrrev_b32_e32 v4, 26, v4
	v_add_u32_e32 v4, v2, v4
	v_lshlrev_b32_e32 v3, 3, v13
	v_ashrrev_i32_e32 v14, 6, v4
	v_and_b32_e32 v4, 0xc0, v4
	v_and_b32_e32 v3, -16, v3
	v_sub_u32_e32 v2, v2, v4
	v_add_u32_e32 v3, v14, v3
	v_ashrrev_i16_sdwa v2, v225, sext(v2) dst_sel:DWORD dst_unused:UNUSED_PAD src0_sel:DWORD src1_sel:BYTE_0
	v_lshlrev_b32_e32 v5, 5, v13
	v_bfe_i32 v15, v2, 0, 16
	v_lshlrev_b32_e32 v2, 1, v3
	v_lshrrev_b32_e32 v4, 2, v3
	v_and_b32_e32 v6, 3, v14
	v_and_b32_e32 v5, 32, v5
	v_and_b32_e32 v2, 24, v2
	v_and_b32_e32 v4, 4, v4
	v_and_or_b32 v6, v3, s4, v6
	s_addc_u32 s17, s71, s5
	v_or3_b32 v2, v6, v4, v2
	v_add_lshl_u32 v4, v5, v15, 1
	v_lshl_add_u32 v166, v2, 10, v4
	v_lshl_add_u32 v164, v3, 10, v4
	s_ashr_i32 s4, s26, 31
	s_lshr_b32 s4, s4, 30
	s_add_i32 s4, s26, s4
	s_ashr_i32 s4, s4, 2
	s_ashr_i32 s47, s6, 6
	s_ashr_i32 s46, s6, 8
	s_lshl_b32 s45, s47, 10
	v_mov_b32_e32 v167, v1
	v_mov_b32_e32 v163, v1
	v_mov_b32_e32 v165, v1
	v_lshlrev_b32_e32 v2, 2, v194
	v_add_u32_e32 v2, 0x20200, v2
	ds_read_b32 v2, v2
	s_waitcnt lgkmcnt(0)
	v_cmp_ge_i32_e32 vcc, s4, v2
	s_and_b32 s5, vcc_lo, 0xfffffffe
	s_bcnt1_i32_b32 s5, s5
	v_mov_b32_e32 v4, s5
	s_add_i32 s101, s5, 1
	v_readlane_b32 s100, v2, s5
	v_readlane_b32 s101, v2, s101
	v_readfirstlane_b32 s64, v4
	s_waitcnt lgkmcnt(0)
	s_mov_b32 s4, s100
	s_lshl_b32 s27, s4, 2
	s_sub_i32 s26, s26, s27
	s_ashr_i32 s27, s26, 31
	s_lshr_b32 s27, s27, 27
	s_add_i32 s27, s26, s27
	s_ashr_i32 s36, s27, 5
	s_lshl_b32 s36, s36, 3
	s_mov_b32 s5, s101
	s_add_i32 s4, s36, s4
	s_sub_i32 s5, s5, s4
	s_min_i32 s5, s5, 8
	s_abs_i32 s37, s5
	v_cvt_f32_u32_e32 v2, s37
	s_sub_i32 s38, 0, s37
	s_andn2_b32 s27, s27, 31
	s_sub_i32 s26, s26, s27
	v_rcp_iflag_f32_e32 v2, v2
	s_abs_i32 s36, s26
	s_xor_b32 s27, s26, s5
	s_ashr_i32 s27, s27, 31
	v_mul_f32_e32 v2, 0x4f7ffffe, v2
	v_cvt_u32_f32_e32 v2, v2
	s_nop 0
	v_readfirstlane_b32 s39, v2
	s_mul_i32 s38, s38, s39
	s_mul_hi_u32 s38, s39, s38
	s_add_i32 s39, s39, s38
	s_mul_hi_u32 s38, s36, s39
	s_mul_i32 s39, s38, s37
	s_sub_i32 s36, s36, s39
	s_add_i32 s39, s38, 1
	s_sub_i32 s40, s36, s37
	s_cmp_ge_u32 s36, s37
	s_cselect_b32 s38, s39, s38
	s_cselect_b32 s36, s40, s36
	s_add_i32 s39, s38, 1
	s_cmp_ge_u32 s36, s37
	s_cselect_b32 s36, s39, s38
	s_xor_b32 s36, s36, s27
	s_sub_i32 s66, s36, s27
	s_mul_i32 s5, s66, s5
	s_sub_i32 s5, s26, s5
	s_add_i32 s62, s4, s5
	s_ashr_i32 s63, s62, 31
	s_ashr_i32 s65, s64, 31
	s_lshl_b64 s[4:5], s[62:63], 18
	s_lshl_b64 s[26:27], s[64:65], 20
	s_add_u32 s36, s16, s26
	s_addc_u32 s37, s17, s27
	s_ashr_i32 s67, s66, 31
	s_lshl_b64 s[26:27], s[66:67], 18
	s_add_u32 s36, s36, s26
	s_addc_u32 s37, s37, s27
	s_add_i32 s63, s45, 0
	s_add_i32 m0, s63, 0x10000
	v_lshl_add_u64 v[2:3], s[36:37], 0, v[0:1]
	global_load_lds_dwordx4 v0, s[36:37]
	s_add_i32 m0, s63, 0x12000
	s_add_u32 s26, s36, 0x20000
	global_load_lds_dwordx4 v166, s[36:37]
	s_addc_u32 s27, s37, 0
	s_add_i32 m0, s63, 0x14000
	v_lshl_add_u64 v[4:5], s[36:37], 0, v[166:167]
	global_load_lds_dwordx4 v0, s[26:27]
	s_add_i32 m0, s63, 0x16000
	s_nop 0
	global_load_lds_dwordx4 v166, s[26:27]
	s_add_u32 s26, s14, s4
	s_addc_u32 s27, s15, s5
	s_add_i32 s67, s63, 0x2000
	s_mov_b32 m0, s63
	s_add_u32 s4, s26, 0x20000
	global_load_lds_dwordx4 v162, s[26:27]
	s_mov_b32 m0, s67
	s_addc_u32 s5, s27, 0
	s_add_i32 s73, s63, 0x4000
	global_load_lds_dwordx4 v164, s[26:27]
	s_mov_b32 m0, s73
	s_add_i32 s75, s63, 0x6000
	global_load_lds_dwordx4 v162, s[4:5]
	s_mov_b32 m0, s75
	s_cmp_eq_u32 s46, 1
	global_load_lds_dwordx4 v164, s[4:5]
	v_lshl_add_u64 v[6:7], s[26:27], 0, v[162:163]
	v_lshl_add_u64 v[8:9], s[26:27], 0, v[164:165]
	s_cselect_b64 s[38:39], -1, 0
	s_cmp_lg_u32 s46, 1
	s_cbranch_scc1 .LBB0_37
	s_barrier

.LBB0_45:
	s_mov_b64 s[54:55], 0
	s_and_b64 vcc, exec, s[60:61]
	s_cbranch_vccz .LBB0_48
	s_ashr_i32 s6, s4, 31
	v_mov_b32_e32 v2, s4
	v_mov_b32_e32 v3, s6
	v_cmp_ge_i64_e32 vcc, s[58:59], v[2:3]
	s_cbranch_vccnz .LBB0_48
	s_ashr_i32 s4, s58, 31
	s_lshr_b32 s4, s4, 30
	s_add_i32 s4, s58, s4
	s_ashr_i32 s4, s4, 2
	v_lshlrev_b32_e32 v2, 2, v194
	v_add_u32_e32 v2, 0x20200, v2
	ds_read_b32 v2, v2
	s_waitcnt lgkmcnt(0)
	v_cmp_ge_i32_e32 vcc, s4, v2
	s_and_b32 s6, vcc_lo, 0xfffffffe
	s_bcnt1_i32_b32 s6, s6
	v_mov_b32_e32 v4, s6
	s_add_i32 s101, s6, 1
	v_readlane_b32 s100, v2, s6
	v_readlane_b32 s101, v2, s101
	s_waitcnt lgkmcnt(0)
	s_mov_b32 s4, s100
	s_lshl_b32 s48, s4, 2
	s_sub_i32 s48, s58, s48
	s_ashr_i32 s49, s48, 31
	s_lshr_b32 s49, s49, 27
	s_add_i32 s49, s48, s49
	s_ashr_i32 s50, s49, 5
	s_lshl_b32 s50, s50, 3
	s_mov_b32 s6, s101
	s_add_i32 s4, s50, s4
	s_sub_i32 s6, s6, s4
	s_min_i32 s6, s6, 8
	s_abs_i32 s51, s6
	v_cvt_f32_u32_e32 v2, s51
	s_sub_i32 s52, 0, s51
	s_andn2_b32 s49, s49, 31
	s_sub_i32 s49, s48, s49
	v_rcp_iflag_f32_e32 v2, v2
	s_abs_i32 s50, s49
	s_xor_b32 s48, s49, s6
	s_ashr_i32 s48, s48, 31
	v_mul_f32_e32 v2, 0x4f7ffffe, v2
	v_cvt_u32_f32_e32 v2, v2
	s_nop 0
	v_readfirstlane_b32 s53, v2
	s_mul_i32 s52, s52, s53
	s_mul_hi_u32 s52, s53, s52
	s_add_i32 s53, s53, s52
	s_mul_hi_u32 s52, s50, s53
	s_mul_i32 s53, s52, s51
	s_sub_i32 s50, s50, s53
	s_add_i32 s53, s52, 1
	s_sub_i32 s54, s50, s51
	s_cmp_ge_u32 s50, s51
	s_cselect_b32 s52, s53, s52
	s_cselect_b32 s50, s54, s50
	s_add_i32 s53, s52, 1
	s_cmp_ge_u32 s50, s51
	s_cselect_b32 s50, s53, s52
	s_xor_b32 s50, s50, s48
	s_sub_i32 s48, s50, s48
	s_mul_i32 s6, s48, s6
	s_sub_i32 s6, s49, s6
	s_add_i32 s50, s4, s6
	v_readfirstlane_b32 s52, v4
	s_mov_b64 s[54:55], -1

.LBB0_141:
	s_ashr_i32 s41, s40, 31
	s_mov_b64 s[36:37], 0
	s_and_b64 vcc, exec, s[38:39]
	s_mov_b32 s78, s80
	s_mov_b32 s48, s7
	s_cbranch_vccz .LBB0_144
	s_waitcnt vmcnt(0)
	v_mov_b64_e32 v[2:3], s[40:41]
	v_cmp_ge_i64_e32 vcc, s[26:27], v[2:3]
	s_mov_b32 s48, s7
	s_mov_b32 s78, s80
	s_cbranch_vccnz .LBB0_144
	s_ashr_i32 s4, s26, 31
	s_lshr_b32 s4, s4, 29
	s_add_i32 s4, s26, s4
	s_ashr_i32 s4, s4, 3
	s_mov_b64 s[36:37], -1
	v_lshlrev_b32_e32 v2, 2, v194
	v_add_u32_e32 v2, 0x20200, v2
	ds_read_b32 v2, v2
	s_waitcnt lgkmcnt(0)
	v_cmp_ge_i32_e32 vcc, s4, v2
	s_and_b32 s5, vcc_lo, 0xfffffffe
	s_bcnt1_i32_b32 s5, s5
	v_mov_b32_e32 v0, s5
	s_add_i32 s101, s5, 1
	v_readlane_b32 s100, v2, s5
	v_readlane_b32 s101, v2, s101
	v_readfirstlane_b32 s48, v0
	s_waitcnt lgkmcnt(0)
	s_mov_b32 s4, s100
	s_lshl_b32 s6, s4, 3
	s_sub_i32 s6, s26, s6
	s_ashr_i32 s14, s6, 31
	s_lshr_b32 s14, s14, 27
	s_add_i32 s14, s6, s14
	s_ashr_i32 s15, s14, 5
	s_lshl_b32 s15, s15, 2
	s_mov_b32 s5, s101
	s_add_i32 s4, s15, s4
	s_sub_i32 s5, s5, s4
	s_min_i32 s5, s5, 4
	s_andn2_b32 s14, s14, 31
	s_sub_i32 s6, s6, s14
	s_lshr_b32 s100, s5, 1
	s_lshr_b32 s100, s6, s100
	s_mul_i32 s101, s6, 22
	s_lshr_b32 s101, s101, 6
	s_cmp_eq_u32 s5, 3
	s_cselect_b32 s100, s101, s100
	s_mul_i32 s101, s100, s5
	s_sub_i32 s101, s6, s101
	s_add_i32 s78, s4, s101

.LBB0_151:
	s_mov_b64 s[36:37], 0
	s_and_b64 vcc, exec, s[50:51]
	s_cbranch_vccz .LBB0_154
	v_mov_b64_e32 v[4:5], s[40:41]
	v_cmp_ge_i64_e32 vcc, s[26:27], v[4:5]
	s_cbranch_vccnz .LBB0_154
	s_ashr_i32 s4, s26, 31
	s_lshr_b32 s4, s4, 29
	s_add_i32 s4, s26, s4
	s_ashr_i32 s4, s4, 3
	s_mov_b64 s[36:37], -1
	s_waitcnt vmcnt(14)
	v_lshlrev_b32_e32 v4, 2, v194
	v_add_u32_e32 v4, 0x20200, v4
	ds_read_b32 v4, v4
	s_waitcnt lgkmcnt(0)
	v_cmp_ge_i32_e32 vcc, s4, v4
	s_and_b32 s6, vcc_lo, 0xfffffffe
	s_bcnt1_i32_b32 s6, s6
	v_mov_b32_e32 v3, s6
	s_add_i32 s101, s6, 1
	v_readlane_b32 s100, v4, s6
	v_readlane_b32 s101, v4, s101
	v_readfirstlane_b32 s48, v3
	s_waitcnt lgkmcnt(0)
	s_mov_b32 s4, s100
	s_lshl_b32 s14, s4, 3
	s_sub_i32 s14, s26, s14
	s_ashr_i32 s15, s14, 31
	s_lshr_b32 s15, s15, 27
	s_add_i32 s15, s14, s15
	s_ashr_i32 s16, s15, 5
	s_lshl_b32 s16, s16, 2
	s_mov_b32 s6, s101
	s_add_i32 s4, s16, s4
	s_sub_i32 s6, s6, s4
	s_min_i32 s6, s6, 4
	s_andn2_b32 s15, s15, 31
	s_sub_i32 s14, s14, s15
	s_lshr_b32 s100, s6, 1
	s_lshr_b32 s100, s14, s100
	s_mul_i32 s101, s14, 22
	s_lshr_b32 s101, s101, 6
	s_cmp_eq_u32 s6, 3
	s_cselect_b32 s100, s101, s100
	s_mul_i32 s101, s100, s6
	s_sub_i32 s101, s14, s101
	s_add_i32 s78, s4, s101

.LBB0_161:
	s_mov_b64 s[36:37], 0
	s_and_b64 vcc, exec, s[50:51]
	s_cbranch_vccz .LBB0_164
	v_mov_b64_e32 v[4:5], s[40:41]
	v_cmp_ge_i64_e32 vcc, s[26:27], v[4:5]
	s_cbranch_vccnz .LBB0_164
	s_ashr_i32 s4, s26, 31
	s_lshr_b32 s4, s4, 29
	s_add_i32 s4, s26, s4
	s_ashr_i32 s4, s4, 3
	s_mov_b64 s[36:37], -1
	s_waitcnt vmcnt(14)
	v_lshlrev_b32_e32 v4, 2, v194
	v_add_u32_e32 v4, 0x20200, v4
	ds_read_b32 v4, v4
	s_waitcnt lgkmcnt(0)
	v_cmp_ge_i32_e32 vcc, s4, v4
	s_and_b32 s6, vcc_lo, 0xfffffffe
	s_bcnt1_i32_b32 s6, s6
	v_mov_b32_e32 v6, s6
	s_add_i32 s101, s6, 1
	v_readlane_b32 s100, v4, s6
	v_readlane_b32 s101, v4, s101
	v_readfirstlane_b32 s48, v6
	s_waitcnt lgkmcnt(0)
	s_mov_b32 s4, s100
	s_lshl_b32 s14, s4, 3
	s_sub_i32 s14, s26, s14
	s_ashr_i32 s15, s14, 31
	s_lshr_b32 s15, s15, 27
	s_add_i32 s15, s14, s15
	s_ashr_i32 s16, s15, 5
	s_lshl_b32 s16, s16, 2
	s_mov_b32 s6, s101
	s_add_i32 s4, s16, s4
	s_sub_i32 s6, s6, s4
	s_min_i32 s6, s6, 4
	s_andn2_b32 s15, s15, 31
	s_sub_i32 s14, s14, s15
	s_lshr_b32 s100, s6, 1
	s_lshr_b32 s100, s14, s100
	s_mul_i32 s101, s14, 22
	s_lshr_b32 s101, s101, 6
	s_cmp_eq_u32 s6, 3
	s_cselect_b32 s100, s101, s100
	s_mul_i32 s101, s100, s6
	s_sub_i32 s101, s14, s101
	s_add_i32 s78, s4, s101

.LBB0_171:
	s_mov_b64 s[36:37], 0
	s_and_b64 vcc, exec, s[50:51]
	s_cbranch_vccz .LBB0_174
	s_waitcnt vmcnt(14)
	v_mov_b64_e32 v[6:7], s[40:41]
	v_cmp_ge_i64_e32 vcc, s[26:27], v[6:7]
	s_cbranch_vccnz .LBB0_174
	s_ashr_i32 s4, s26, 31
	s_lshr_b32 s4, s4, 29
	s_add_i32 s4, s26, s4
	s_ashr_i32 s4, s4, 3
	s_mov_b64 s[36:37], -1
	v_lshlrev_b32_e32 v6, 2, v194
	v_add_u32_e32 v6, 0x20200, v6
	ds_read_b32 v6, v6
	s_waitcnt lgkmcnt(0)
	v_cmp_ge_i32_e32 vcc, s4, v6
	s_and_b32 s6, vcc_lo, 0xfffffffe
	s_bcnt1_i32_b32 s6, s6
	v_mov_b32_e32 v5, s6
	s_add_i32 s101, s6, 1
	v_readlane_b32 s100, v6, s6
	v_readlane_b32 s101, v6, s101
	v_readfirstlane_b32 s48, v5
	s_waitcnt lgkmcnt(0)
	s_mov_b32 s4, s100
	s_lshl_b32 s14, s4, 3
	s_sub_i32 s14, s26, s14
	s_ashr_i32 s15, s14, 31
	s_lshr_b32 s15, s15, 27
	s_add_i32 s15, s14, s15
	s_ashr_i32 s16, s15, 5
	s_lshl_b32 s16, s16, 2
	s_mov_b32 s6, s101
	s_add_i32 s4, s16, s4
	s_sub_i32 s6, s6, s4
	s_min_i32 s6, s6, 4
	s_andn2_b32 s15, s15, 31
	s_sub_i32 s14, s14, s15
	s_lshr_b32 s100, s6, 1
	s_lshr_b32 s100, s14, s100
	s_mul_i32 s101, s14, 22
	s_lshr_b32 s101, s101, 6
	s_cmp_eq_u32 s6, 3
	s_cselect_b32 s100, s101, s100
	s_mul_i32 s101, s100, s6
	s_sub_i32 s101, s14, s101
	s_add_i32 s78, s4, s101

.LBB0_181:
	s_mov_b64 s[36:37], 0
	s_and_b64 vcc, exec, s[50:51]
	s_cbranch_vccz .LBB0_184
	s_waitcnt vmcnt(14)
	v_mov_b64_e32 v[6:7], s[40:41]
	v_cmp_ge_i64_e32 vcc, s[26:27], v[6:7]
	s_cbranch_vccnz .LBB0_184
	s_ashr_i32 s4, s26, 31
	s_lshr_b32 s4, s4, 29
	s_add_i32 s4, s26, s4
	s_ashr_i32 s4, s4, 3
	s_mov_b64 s[36:37], -1
	v_lshlrev_b32_e32 v6, 2, v194
	v_add_u32_e32 v6, 0x20200, v6
	ds_read_b32 v6, v6
	s_waitcnt lgkmcnt(0)
	v_cmp_ge_i32_e32 vcc, s4, v6
	s_and_b32 s6, vcc_lo, 0xfffffffe
	s_bcnt1_i32_b32 s6, s6
	v_mov_b32_e32 v8, s6
	s_add_i32 s101, s6, 1
	v_readlane_b32 s100, v6, s6
	v_readlane_b32 s101, v6, s101
	v_readfirstlane_b32 s48, v8
	s_waitcnt lgkmcnt(0)
	s_mov_b32 s4, s100
	s_lshl_b32 s14, s4, 3
	s_sub_i32 s14, s26, s14
	s_ashr_i32 s15, s14, 31
	s_lshr_b32 s15, s15, 27
	s_add_i32 s15, s14, s15
	s_ashr_i32 s16, s15, 5
	s_lshl_b32 s16, s16, 2
	s_mov_b32 s6, s101
	s_add_i32 s4, s16, s4
	s_sub_i32 s6, s6, s4
	s_min_i32 s6, s6, 4
	s_andn2_b32 s15, s15, 31
	s_sub_i32 s14, s14, s15
	s_lshr_b32 s100, s6, 1
	s_lshr_b32 s100, s14, s100
	s_mul_i32 s101, s14, 22
	s_lshr_b32 s101, s101, 6
	s_cmp_eq_u32 s6, 3
	s_cselect_b32 s100, s101, s100
	s_mul_i32 s101, s100, s6
	s_sub_i32 s101, s14, s101
	s_add_i32 s78, s4, s101

.LBB0_191:
	s_mov_b64 s[36:37], 0
	s_and_b64 vcc, exec, s[50:51]
	s_cbranch_vccz .LBB0_194
	v_mov_b64_e32 v[8:9], s[40:41]
	v_cmp_ge_i64_e32 vcc, s[26:27], v[8:9]
	s_cbranch_vccnz .LBB0_194
	s_ashr_i32 s4, s26, 31
	s_lshr_b32 s4, s4, 29
	s_add_i32 s4, s26, s4
	s_ashr_i32 s4, s4, 3
	s_mov_b64 s[36:37], -1
	s_waitcnt vmcnt(13)
	v_lshlrev_b32_e32 v8, 2, v194
	v_add_u32_e32 v8, 0x20200, v8
	ds_read_b32 v8, v8
	s_waitcnt lgkmcnt(0)
	v_cmp_ge_i32_e32 vcc, s4, v8
	s_and_b32 s6, vcc_lo, 0xfffffffe
	s_bcnt1_i32_b32 s6, s6
	v_mov_b32_e32 v7, s6
	s_add_i32 s101, s6, 1
	v_readlane_b32 s100, v8, s6
	v_readlane_b32 s101, v8, s101
	v_readfirstlane_b32 s48, v7
	s_waitcnt lgkmcnt(0)
	s_mov_b32 s4, s100
	s_lshl_b32 s14, s4, 3
	s_sub_i32 s14, s26, s14
	s_ashr_i32 s15, s14, 31
	s_lshr_b32 s15, s15, 27
	s_add_i32 s15, s14, s15
	s_ashr_i32 s16, s15, 5
	s_lshl_b32 s16, s16, 2
	s_mov_b32 s6, s101
	s_add_i32 s4, s16, s4
	s_sub_i32 s6, s6, s4
	s_min_i32 s6, s6, 4
	s_andn2_b32 s15, s15, 31
	s_sub_i32 s14, s14, s15
	s_lshr_b32 s100, s6, 1
	s_lshr_b32 s100, s14, s100
	s_mul_i32 s101, s14, 22
	s_lshr_b32 s101, s101, 6
	s_cmp_eq_u32 s6, 3
	s_cselect_b32 s100, s101, s100
	s_mul_i32 s101, s100, s6
	s_sub_i32 s101, s14, s101
	s_add_i32 s78, s4, s101

.LBB0_201:
	s_mov_b64 s[36:37], 0
	s_and_b64 vcc, exec, s[50:51]
	s_cbranch_vccz .LBB0_204
	v_mov_b64_e32 v[8:9], s[40:41]
	v_cmp_ge_i64_e32 vcc, s[26:27], v[8:9]
	s_cbranch_vccnz .LBB0_204
	s_ashr_i32 s4, s26, 31
	s_lshr_b32 s4, s4, 29
	s_add_i32 s4, s26, s4
	s_ashr_i32 s4, s4, 3
	s_mov_b64 s[36:37], -1
	s_waitcnt vmcnt(13)
	v_lshlrev_b32_e32 v8, 2, v194
	v_add_u32_e32 v8, 0x20200, v8
	ds_read_b32 v8, v8
	s_waitcnt lgkmcnt(0)
	v_cmp_ge_i32_e32 vcc, s4, v8
	s_and_b32 s6, vcc_lo, 0xfffffffe
	s_bcnt1_i32_b32 s6, s6
	v_mov_b32_e32 v10, s6
	s_add_i32 s101, s6, 1
	v_readlane_b32 s100, v8, s6
	v_readlane_b32 s101, v8, s101
	v_readfirstlane_b32 s48, v10
	s_waitcnt lgkmcnt(0)
	s_mov_b32 s4, s100
	s_lshl_b32 s14, s4, 3
	s_sub_i32 s14, s26, s14
	s_ashr_i32 s15, s14, 31
	s_lshr_b32 s15, s15, 27
	s_add_i32 s15, s14, s15
	s_ashr_i32 s16, s15, 5
	s_lshl_b32 s16, s16, 2
	s_mov_b32 s6, s101
	s_add_i32 s4, s16, s4
	s_sub_i32 s6, s6, s4
	s_min_i32 s6, s6, 4
	s_andn2_b32 s15, s15, 31
	s_sub_i32 s14, s14, s15
	s_lshr_b32 s100, s6, 1
	s_lshr_b32 s100, s14, s100
	s_mul_i32 s101, s14, 22
	s_lshr_b32 s101, s101, 6
	s_cmp_eq_u32 s6, 3
	s_cselect_b32 s100, s101, s100
	s_mul_i32 s101, s100, s6
	s_sub_i32 s101, s14, s101
	s_add_i32 s78, s4, s101

.LBB0_211:
	s_mov_b64 s[36:37], 0
	s_and_b64 vcc, exec, s[50:51]
	s_cbranch_vccz .LBB0_214
	s_waitcnt vmcnt(13)
	v_mov_b64_e32 v[10:11], s[40:41]
	v_cmp_ge_i64_e32 vcc, s[26:27], v[10:11]
	s_cbranch_vccnz .LBB0_214
	s_ashr_i32 s4, s26, 31
	s_lshr_b32 s4, s4, 29
	s_add_i32 s4, s26, s4
	s_ashr_i32 s4, s4, 3
	s_mov_b64 s[36:37], -1
	v_lshlrev_b32_e32 v10, 2, v194
	v_add_u32_e32 v10, 0x20200, v10
	ds_read_b32 v10, v10
	s_waitcnt lgkmcnt(0)
	v_cmp_ge_i32_e32 vcc, s4, v10
	s_and_b32 s6, vcc_lo, 0xfffffffe
	s_bcnt1_i32_b32 s6, s6
	v_mov_b32_e32 v9, s6
	s_add_i32 s101, s6, 1
	v_readlane_b32 s100, v10, s6
	v_readlane_b32 s101, v10, s101
	v_readfirstlane_b32 s48, v9
	s_waitcnt lgkmcnt(0)
	s_mov_b32 s4, s100
	s_lshl_b32 s14, s4, 3
	s_sub_i32 s14, s26, s14
	s_ashr_i32 s15, s14, 31
	s_lshr_b32 s15, s15, 27
	s_add_i32 s15, s14, s15
	s_ashr_i32 s16, s15, 5
	s_lshl_b32 s16, s16, 2
	s_mov_b32 s6, s101
	s_add_i32 s4, s16, s4
	s_sub_i32 s6, s6, s4
	s_min_i32 s6, s6, 4
	s_andn2_b32 s15, s15, 31
	s_sub_i32 s14, s14, s15
	s_lshr_b32 s100, s6, 1
	s_lshr_b32 s100, s14, s100
	s_mul_i32 s101, s14, 22
	s_lshr_b32 s101, s101, 6
	s_cmp_eq_u32 s6, 3
	s_cselect_b32 s100, s101, s100
	s_mul_i32 s101, s100, s6
	s_sub_i32 s101, s14, s101
	s_add_i32 s78, s4, s101

.LBB0_221:
	s_mov_b64 s[36:37], 0
	s_and_b64 vcc, exec, s[38:39]
	s_cbranch_vccz .LBB0_224
	s_waitcnt vmcnt(13)
	v_mov_b64_e32 v[10:11], s[40:41]
	v_cmp_ge_i64_e32 vcc, s[26:27], v[10:11]
	s_cbranch_vccnz .LBB0_224
	s_ashr_i32 s4, s26, 31
	s_lshr_b32 s4, s4, 29
	s_add_i32 s4, s26, s4
	s_ashr_i32 s4, s4, 3
	s_mov_b64 s[36:37], -1
	v_lshlrev_b32_e32 v10, 2, v194
	v_add_u32_e32 v10, 0x20200, v10
	ds_read_b32 v10, v10
	s_waitcnt lgkmcnt(0)
	v_cmp_ge_i32_e32 vcc, s4, v10
	s_and_b32 s6, vcc_lo, 0xfffffffe
	s_bcnt1_i32_b32 s6, s6
	v_mov_b32_e32 v12, s6
	s_add_i32 s101, s6, 1
	v_readlane_b32 s100, v10, s6
	v_readlane_b32 s101, v10, s101
	v_readfirstlane_b32 s48, v12
	s_waitcnt lgkmcnt(0)
	s_mov_b32 s4, s100
	s_lshl_b32 s14, s4, 3
	s_sub_i32 s14, s26, s14
	s_ashr_i32 s15, s14, 31
	s_lshr_b32 s15, s15, 27
	s_add_i32 s15, s14, s15
	s_ashr_i32 s16, s15, 5
	s_lshl_b32 s16, s16, 2
	s_mov_b32 s6, s101
	s_add_i32 s4, s16, s4
	s_sub_i32 s6, s6, s4
	s_min_i32 s6, s6, 4
	s_andn2_b32 s15, s15, 31
	s_sub_i32 s14, s14, s15
	s_lshr_b32 s100, s6, 1
	s_lshr_b32 s100, s14, s100
	s_mul_i32 s101, s14, 22
	s_lshr_b32 s101, s101, 6
	s_cmp_eq_u32 s6, 3
	s_cselect_b32 s100, s101, s100
	s_mul_i32 s101, s100, s6
	s_sub_i32 s101, s14, s101
	s_add_i32 s78, s4, s101

.LBB0_231:
	v_lshlrev_b32_e32 v188, 4, v192
	v_and_b32_e32 v189, 15, v194
	s_and_b64 vcc, exec, s[38:39]
	s_cbranch_vccz .LBB0_257
	s_ashr_i32 s5, s4, 31
	v_mov_b32_e32 v2, s4
	v_mov_b32_e32 v3, s5
	v_cmp_ge_i64_e32 vcc, s[26:27], v[2:3]
	s_cbranch_vccnz .LBB0_257
	v_ashrrev_i32_e32 v0, 31, v192
	v_lshrrev_b32_e32 v0, 26, v0
	v_add_u32_e32 v0, v192, v0
	v_ashrrev_i32_e32 v3, 6, v0
	v_ashrrev_i32_e32 v0, 31, v188
	v_lshrrev_b32_e32 v0, 22, v0
	v_add_u32_e32 v0, v188, v0
	v_and_b32_e32 v0, 0xfffffc00, v0
	v_sub_u32_e32 v2, v188, v0
	v_lshrrev_b32_e32 v0, 4, v2
	v_bitop3_b32 v4, v0, v2, 32 bitop3:0x6c
	v_ashrrev_i32_e32 v2, 31, v2
	v_lshrrev_b32_e32 v2, 26, v2
	v_add_u32_e32 v5, v4, v2
	v_ashrrev_i32_e32 v2, 6, v5
	v_and_b32_e32 v5, 0xc0, v5
	v_sub_u32_e32 v4, v4, v5
	s_add_u32 s40, s46, 0x2e000000
	v_lshlrev_b32_e32 v0, 3, v3
	v_lshlrev_b32_e32 v3, 5, v3
	v_ashrrev_i16_sdwa v4, v225, sext(v4) dst_sel:DWORD dst_unused:UNUSED_PAD src0_sel:DWORD src1_sel:BYTE_0
	s_addc_u32 s41, s47, 0
	s_ashr_i32 s83, s82, 31
	v_and_b32_e32 v0, -16, v0
	v_and_b32_e32 v3, 32, v3
	v_bfe_i32 v4, v4, 0, 16
	v_writelane_b32 v255, s82, 10
	s_lshl_b64 s[4:5], s[82:83], 26
	v_add_u32_e32 v6, v2, v0
	v_add_lshl_u32 v193, v3, v4, 1
	v_add_u32_e32 v3, 0x2000, v188
	v_writelane_b32 v255, s83, 11
	s_add_u32 s82, s49, s4
	v_lshlrev_b32_e32 v5, 1, v6
	v_lshrrev_b32_e32 v7, 2, v6
	v_and_b32_e32 v8, 3, v2
	s_mov_b32 s4, 0x3fffe0
	v_ashrrev_i32_e32 v4, 31, v3
	v_and_b32_e32 v5, 24, v5
	v_and_b32_e32 v7, 4, v7
	v_and_or_b32 v6, v6, s4, v8
	v_lshrrev_b32_e32 v4, 22, v4
	v_or3_b32 v5, v6, v7, v5
	v_add_u32_e32 v4, v3, v4
	v_lshl_add_u32 v162, v5, 10, v193
	v_ashrrev_i32_e32 v5, 10, v4
	v_mul_i32_i24_e32 v4, 0x400, v5
	v_sub_u32_e32 v3, v3, v4
	v_lshrrev_b32_e32 v4, 4, v3
	v_bitop3_b32 v6, v4, v3, 32 bitop3:0x6c
	v_ashrrev_i32_e32 v4, 31, v6
	v_lshrrev_b32_e32 v4, 26, v4
	v_lshlrev_b32_e32 v3, 3, v5
	v_add_u32_e32 v7, v6, v4
	v_and_b32_e32 v3, -16, v3
	v_ashrrev_i32_e32 v4, 6, v7
	v_and_b32_e32 v7, 0xc0, v7
	v_add_u32_e32 v8, v4, v3
	v_sub_u32_e32 v6, v6, v7
	v_lshlrev_b32_e32 v5, 5, v5
	v_ashrrev_i16_sdwa v6, v225, sext(v6) dst_sel:DWORD dst_unused:UNUSED_PAD src0_sel:DWORD src1_sel:BYTE_0
	v_lshlrev_b32_e32 v7, 1, v8
	v_lshrrev_b32_e32 v9, 2, v8
	v_and_b32_e32 v10, 3, v4
	s_addc_u32 s83, s73, s5
	v_and_b32_e32 v5, 32, v5
	v_bfe_i32 v6, v6, 0, 16
	v_and_b32_e32 v7, 24, v7
	v_and_b32_e32 v9, 4, v9
	v_and_or_b32 v8, v8, s4, v10
	v_or3_b32 v7, v8, v9, v7
	v_add_lshl_u32 v195, v5, v6, 1
	v_lshl_add_u32 v164, v7, 10, v195
	s_ashr_i32 s4, s26, 31
	s_lshr_b32 s4, s4, 29
	s_add_i32 s4, s26, s4
	s_ashr_i32 s4, s4, 3
	s_ashr_i32 s16, s6, 6
	s_ashr_i32 s15, s6, 8
	s_lshl_b32 s92, s16, 10
	v_lshlrev_b32_e32 v196, 2, v2
	v_lshlrev_b32_e32 v197, 2, v0
	v_lshlrev_b32_e32 v198, 2, v4
	v_lshlrev_b32_e32 v199, 2, v3
	v_mov_b32_e32 v163, v1
	v_mov_b32_e32 v165, v1
	v_lshlrev_b32_e32 v6, 2, v194
	v_add_u32_e32 v6, 0x20200, v6
	ds_read_b32 v6, v6
	s_waitcnt lgkmcnt(0)
	v_cmp_ge_i32_e32 vcc, s4, v6
	s_and_b32 s5, vcc_lo, 0xfffffffe
	s_bcnt1_i32_b32 s5, s5
	v_mov_b32_e32 v5, s5
	s_add_i32 s101, s5, 1
	v_readlane_b32 s100, v6, s5
	v_readlane_b32 s101, v6, s101
	v_readfirstlane_b32 s68, v5
	s_waitcnt lgkmcnt(0)
	s_mov_b32 s4, s100
	s_lshl_b32 s14, s4, 3
	s_sub_i32 s14, s26, s14
	s_ashr_i32 s17, s14, 31
	s_lshr_b32 s17, s17, 27
	s_add_i32 s17, s14, s17
	s_ashr_i32 s26, s17, 5
	s_lshl_b32 s26, s26, 2
	s_mov_b32 s5, s101
	s_add_i32 s4, s26, s4
	s_sub_i32 s5, s5, s4
	s_min_i32 s5, s5, 4
	s_andn2_b32 s17, s17, 31
	s_sub_i32 s14, s14, s17
	s_lshr_b32 s100, s5, 1
	s_lshr_b32 s100, s14, s100
	s_mul_i32 s101, s14, 22
	s_lshr_b32 s101, s101, 6
	s_cmp_eq_u32 s5, 3
	s_cselect_b32 s100, s101, s100
	s_mul_i32 s101, s100, s5
	s_sub_i32 s5, s14, s101
	s_mov_b32 s66, s100
	s_add_i32 s14, 0, 0x21000
	v_add3_u32 v0, s14, v196, v197
	ds_read_b32 v0, v0
	s_ashr_i32 s69, s68, 31
	s_ashr_i32 s67, s66, 31
	s_add_i32 s75, s4, s5
	s_lshl_b64 s[4:5], s[68:69], 21
	s_waitcnt lgkmcnt(0)
	v_lshl_add_u32 v168, v0, 10, v193
	v_add3_u32 v0, s14, v198, v199
	ds_read_b32 v0, v0
	v_readlane_b32 s14, v254, 52
	s_lshl_b64 s[26:27], s[66:67], 18
	s_add_u32 s4, s82, s4
	s_addc_u32 s5, s83, s5
	s_waitcnt lgkmcnt(0)
	v_lshl_add_u32 v170, v0, 10, v195
	v_add3_u32 v0, s14, v196, v197
	ds_read_b32 v0, v0
	s_add_u32 s26, s4, s26
	s_addc_u32 s27, s5, s27
	s_add_i32 s93, s92, 0
	s_add_i32 m0, s93, 0x10000
	s_waitcnt lgkmcnt(0)
	v_lshl_add_u32 v172, v0, 10, v193
	v_add3_u32 v0, s14, v198, v199
	ds_read_b32 v0, v0
	global_load_lds_dwordx4 v162, s[26:27]
	s_add_i32 m0, s93, 0x12000
	s_add_u32 s4, s26, 0x20000
	global_load_lds_dwordx4 v164, s[26:27]
	s_addc_u32 s5, s27, 0
	s_add_i32 m0, s93, 0x14000
	s_add_i32 s79, s93, 0x2000
	global_load_lds_dwordx4 v162, s[4:5]
	s_add_i32 m0, s93, 0x16000
	s_add_i32 s84, s93, 0x4000
	global_load_lds_dwordx4 v164, s[4:5]
	s_mov_b32 m0, s93
	s_add_i32 s85, s93, 0x6000
	global_load_lds_dwordx4 v168, s[40:41]
	s_mov_b32 m0, s79
	s_waitcnt lgkmcnt(0)
	v_lshl_add_u32 v174, v0, 10, v195
	global_load_lds_dwordx4 v170, s[40:41]
	s_mov_b32 m0, s84
	s_cmp_eq_u32 s15, 1
	global_load_lds_dwordx4 v172, s[40:41]
	s_mov_b32 m0, s85
	v_lshl_add_u64 v[2:3], s[26:27], 0, v[162:163]
	global_load_lds_dwordx4 v174, s[40:41]
	v_lshl_add_u64 v[4:5], s[26:27], 0, v[164:165]
	s_cselect_b64 s[42:43], -1, 0
	s_cmp_lg_u32 s15, 1
	s_cbranch_scc1 .LBB0_235
	s_barrier

.LBB0_243:
	s_mov_b64 s[70:71], 0
	s_and_b64 vcc, exec, s[38:39]
	s_cbranch_vccz .LBB0_246
	s_ashr_i32 s6, s4, 31
	v_mov_b32_e32 v2, s4
	v_mov_b32_e32 v3, s6
	v_cmp_ge_i64_e32 vcc, s[36:37], v[2:3]
	s_cbranch_vccnz .LBB0_246
	s_ashr_i32 s4, s36, 31
	s_lshr_b32 s4, s4, 29
	s_add_i32 s4, s36, s4
	s_ashr_i32 s4, s4, 3
	s_mov_b64 s[70:71], -1
	v_lshlrev_b32_e32 v2, 2, v194
	v_add_u32_e32 v2, 0x20200, v2
	ds_read_b32 v2, v2
	s_waitcnt lgkmcnt(0)
	v_cmp_ge_i32_e32 vcc, s4, v2
	s_and_b32 s6, vcc_lo, 0xfffffffe
	s_bcnt1_i32_b32 s6, s6
	v_mov_b32_e32 v0, s6
	s_add_i32 s101, s6, 1
	v_readlane_b32 s100, v2, s6
	v_readlane_b32 s101, v2, s101
	v_readfirstlane_b32 s62, v0
	s_waitcnt lgkmcnt(0)
	s_mov_b32 s4, s100
	s_lshl_b32 s30, s4, 3
	s_sub_i32 s30, s36, s30
	s_ashr_i32 s31, s30, 31
	s_lshr_b32 s31, s31, 27
	s_add_i32 s31, s30, s31
	s_ashr_i32 s36, s31, 5
	s_lshl_b32 s36, s36, 2
	s_mov_b32 s6, s101
	s_add_i32 s4, s36, s4
	s_sub_i32 s6, s6, s4
	s_min_i32 s6, s6, 4
	s_andn2_b32 s31, s31, 31
	s_sub_i32 s30, s30, s31
	s_lshr_b32 s100, s6, 1
	s_lshr_b32 s100, s30, s100
	s_mul_i32 s101, s30, 22
	s_lshr_b32 s101, s101, 6
	s_cmp_eq_u32 s6, 3
	s_cselect_b32 s100, s101, s100
	s_mul_i32 s101, s100, s6
	s_sub_i32 s6, s30, s101
	s_mov_b32 s60, s100
	s_add_i32 s30, s4, s6
